# speedup vs baseline: 1.0438x; 1.0438x over previous
_Z6k_histPKfS0_S0_PfPiS1_:
	s_load_dwordx4 s[4:7], s[0:1], 0x0
	s_load_dwordx4 s[8:11], s[0:1], 0x10
	s_load_dwordx4 s[12:15], s[0:1], 0x20
	v_and_b32_e32 v1, 63, v0
	v_readfirstlane_b32 s3, v0
	v_mov_b32_e32 v20, 0
	v_mov_b32_e32 v21, 0
	v_mov_b32_e32 v22, 0
	v_mov_b32_e32 v23, 0
	v_lshl_add_u32 v19, v0, 4, 32
	s_lshr_b32 s3, s3, 6
	ds_write_b128 v19, v[20:23]
	ds_write_b128 v19, v[20:23] offset:16384
	s_cmp_lg_u32 s3, 0
	s_cbranch_scc1 .Lh_zero_done
	ds_write_b128 v19, v[20:23] offset:32768
.Lh_zero_done:
	s_and_b32 s16, s3, 7
	s_lshr_b32 s17, s3, 3
	s_and_b32 s18, s2, 31
	s_lshr_b32 s19, s2, 5
	s_lshl_b32 s18, s18, 13
	s_lshl_b32 s20, s16, 10
	s_add_u32 s18, s18, s20
	v_lshl_add_u32 v18, v1, 4, s18
	s_mul_i32 s21, s19, 3
	s_lshl_b32 s22, s19, 18
	s_lshl_b32 s21, s21, 18
	s_or_b32 s23, s2, s3
	s_waitcnt lgkmcnt(0)
	s_cmp_lg_u32 s23, 0
	s_cbranch_scc1 .Lh_no_out
	s_mov_b64 exec, 1
	global_store_dword v20, v20, s[14:15]
	s_mov_b64 exec, -1
.Lh_no_out:
	s_cmp_eq_u32 s17, 0
	s_cselect_b32 s4, s4, s6
	s_cselect_b32 s5, s5, s7
	s_add_u32 s24, s8, s22
	s_addc_u32 s25, s9, 0
	s_add_u32 s4, s4, s21
	s_addc_u32 s5, s5, 0
	global_load_dwordx4 v[14:17], v18, s[24:25] nt
	global_load_dwordx4 v[2:5], v18, s[4:5] nt
	s_add_u32 s6, s4, 0x40000
	s_addc_u32 s7, s5, 0
	s_add_u32 s8, s4, 0x80000
	s_addc_u32 s9, s5, 0
	s_barrier
	global_load_dwordx4 v[6:9], v18, s[6:7] nt
	s_barrier
	global_load_dwordx4 v[10:13], v18, s[8:9] nt
	s_mul_i32 s46, s3, 0xc00
	s_add_u32 s46, s46, 0x8420
	v_lshl_add_u32 v26, v1, 2, s46
	v_and_b32_e32 v38, 15, v0
	s_mul_i32 s58, s17, 0x4200
	s_add_u32 s58, s58, 0x1e0
	v_lshl_add_u32 v38, v38, 2, s58
	v_add_u32_e32 v39, 0x1600, v38
	v_add_u32_e32 v40, 0x2c00, v38
	v_mov_b32_e32 v41, 0x41fc0000
	v_mov_b32_e32 v42, 0xbf38aa3b
	s_mov_b32 s48, 0x3f940000
	s_mov_b32 s51, 0x3fb8aa3b
	s_mov_b32 s42, 0
	s_mov_b32 s43, 0
	s_mov_b32 s44, 0x7fffffff
	s_mov_b32 s45, 0x7fffffff
	s_mov_b32 s47, 0
	s_mul_i32 s58, s3, 0x1600
	s_add_u32 s58, s58, 0x320
	v_lshl_add_u32 v44, v1, 6, s58
	v_bfe_u32 v45, v1, 2, 2
	v_lshlrev_b32_e32 v45, 4, v45
	v_xor_b32_e32 v46, 16, v45
	v_xor_b32_e32 v47, 32, v45
	v_xor_b32_e32 v48, 48, v45
	v_add_u32_e32 v45, v44, v45
	v_add_u32_e32 v46, v44, v46
	v_add_u32_e32 v47, v44, v47
	v_add_u32_e32 v48, v44, v48
	s_mul_i32 s58, s2, 0x600
	s_lshl_b32 s59, s3, 8
	s_add_u32 s58, s58, s59
	s_add_u32 s10, s10, s58
	s_addc_u32 s11, s11, 0
	v_lshlrev_b32_e32 v49, 2, v1
	s_lshl_b32 s58, s2, 2
	s_add_u32 s12, s12, s58
	s_addc_u32 s13, s13, 0
	s_waitcnt vmcnt(3)
	v_cmp_lt_f32_e64 s[26:27], 0.5, v14
	v_cmp_lt_f32_e64 s[28:29], 0.5, v15
	v_cmp_lt_f32_e64 s[30:31], 0.5, v16
	v_cmp_lt_f32_e64 s[32:33], 0.5, v17
	s_cmp_lg_u32 s17, 0
	s_cbranch_scc1 .Lh_no_cnt
	s_bcnt1_i32_b64 s54, s[26:27]
	s_bcnt1_i32_b64 s55, s[28:29]
	s_bcnt1_i32_b64 s56, s[30:31]
	s_bcnt1_i32_b64 s57, s[32:33]
	s_add_i32 s54, s54, s55
	s_add_i32 s56, s56, s57
	s_add_i32 s54, s54, s56
	s_lshl_b32 s55, s16, 2
	v_mov_b32_e32 v36, s55
	v_mov_b32_e32 v37, s54
	s_mov_b64 exec, 1
	ds_write_b32 v36, v37
	s_mov_b64 exec, -1
.Lh_no_cnt:
	s_waitcnt vmcnt(2)
	v_cmp_lt_f32_e64 s[34:35], |v2|, s48
	v_cmp_lt_f32_e64 s[36:37], |v3|, s48
	v_cmp_lt_f32_e64 s[38:39], |v4|, s48
	v_cmp_lt_f32_e64 s[40:41], |v5|, s48
	s_and_b64 s[34:35], s[34:35], s[26:27]
	s_and_b64 s[36:37], s[36:37], s[28:29]
	s_and_b64 s[38:39], s[38:39], s[30:31]
	s_and_b64 s[40:41], s[40:41], s[32:33]
	v_mbcnt_lo_u32_b32 v28, s34, 0
	v_mbcnt_lo_u32_b32 v29, s36, 0
	v_mbcnt_lo_u32_b32 v30, s38, 0
	v_mbcnt_lo_u32_b32 v31, s40, 0
	v_mbcnt_hi_u32_b32 v28, s35, v28
	v_mbcnt_hi_u32_b32 v29, s37, v29
	v_mbcnt_hi_u32_b32 v30, s39, v30
	v_mbcnt_hi_u32_b32 v31, s41, v31
	s_bcnt1_i32_b64 s54, s[34:35]
	s_bcnt1_i32_b64 s55, s[36:37]
	s_bcnt1_i32_b64 s56, s[38:39]
	s_bcnt1_i32_b64 s57, s[40:41]
	s_lshl2_add_u32 s58, s42, s46
	v_lshl_add_u32 v28, v28, 2, s58
	s_lshl2_add_u32 s58, s54, s58
	v_lshl_add_u32 v29, v29, 2, s58
	s_lshl2_add_u32 s58, s55, s58
	v_lshl_add_u32 v30, v30, 2, s58
	s_lshl2_add_u32 s58, s56, s58
	v_lshl_add_u32 v31, v31, 2, s58
	s_add_i32 s54, s54, s55
	s_add_i32 s56, s56, s57
	s_add_i32 s42, s42, s54
	s_add_i32 s42, s42, s56
	s_mov_b64 exec, s[34:35]
	ds_write_b32 v28, v2
	s_mov_b64 exec, s[36:37]
	ds_write_b32 v29, v3
	s_mov_b64 exec, s[38:39]
	ds_write_b32 v30, v4
	s_mov_b64 exec, s[40:41]
	ds_write_b32 v31, v5
	s_mov_b64 exec, -1
	s_branch .Lh_loop_entry
.Lh_stage1:
	s_mov_b32 s47, 1
	s_mov_b32 s44, s42
	s_waitcnt vmcnt(1)
	v_cmp_lt_f32_e64 s[34:35], |v6|, s48
	v_cmp_lt_f32_e64 s[36:37], |v7|, s48
	v_cmp_lt_f32_e64 s[38:39], |v8|, s48
	v_cmp_lt_f32_e64 s[40:41], |v9|, s48
	s_and_b64 s[34:35], s[34:35], s[26:27]
	s_and_b64 s[36:37], s[36:37], s[28:29]
	s_and_b64 s[38:39], s[38:39], s[30:31]
	s_and_b64 s[40:41], s[40:41], s[32:33]
	v_mbcnt_lo_u32_b32 v28, s34, 0
	v_mbcnt_lo_u32_b32 v29, s36, 0
	v_mbcnt_lo_u32_b32 v30, s38, 0
	v_mbcnt_lo_u32_b32 v31, s40, 0
	v_mbcnt_hi_u32_b32 v28, s35, v28
	v_mbcnt_hi_u32_b32 v29, s37, v29
	v_mbcnt_hi_u32_b32 v30, s39, v30
	v_mbcnt_hi_u32_b32 v31, s41, v31
	s_bcnt1_i32_b64 s54, s[34:35]
	s_bcnt1_i32_b64 s55, s[36:37]
	s_bcnt1_i32_b64 s56, s[38:39]
	s_bcnt1_i32_b64 s57, s[40:41]
	s_lshl2_add_u32 s58, s42, s46
	v_lshl_add_u32 v28, v28, 2, s58
	s_lshl2_add_u32 s58, s54, s58
	v_lshl_add_u32 v29, v29, 2, s58
	s_lshl2_add_u32 s58, s55, s58
	v_lshl_add_u32 v30, v30, 2, s58
	s_lshl2_add_u32 s58, s56, s58
	v_lshl_add_u32 v31, v31, 2, s58
	s_add_i32 s54, s54, s55
	s_add_i32 s56, s56, s57
	s_add_i32 s42, s42, s54
	s_add_i32 s42, s42, s56
	s_mov_b64 exec, s[34:35]
	ds_write_b32 v28, v6
	s_mov_b64 exec, s[36:37]
	ds_write_b32 v29, v7
	s_mov_b64 exec, s[38:39]
	ds_write_b32 v30, v8
	s_mov_b64 exec, s[40:41]
	ds_write_b32 v31, v9
	s_mov_b64 exec, -1
	s_branch .Lh_loop_entry
.Lh_stage2:
	s_mov_b32 s47, 2
	s_mov_b32 s45, s42
	s_waitcnt vmcnt(0)
	v_cmp_lt_f32_e64 s[34:35], |v10|, s48
	v_cmp_lt_f32_e64 s[36:37], |v11|, s48
	v_cmp_lt_f32_e64 s[38:39], |v12|, s48
	v_cmp_lt_f32_e64 s[40:41], |v13|, s48
	s_and_b64 s[34:35], s[34:35], s[26:27]
	s_and_b64 s[36:37], s[36:37], s[28:29]
	s_and_b64 s[38:39], s[38:39], s[30:31]
	s_and_b64 s[40:41], s[40:41], s[32:33]
	v_mbcnt_lo_u32_b32 v28, s34, 0
	v_mbcnt_lo_u32_b32 v29, s36, 0
	v_mbcnt_lo_u32_b32 v30, s38, 0
	v_mbcnt_lo_u32_b32 v31, s40, 0
	v_mbcnt_hi_u32_b32 v28, s35, v28
	v_mbcnt_hi_u32_b32 v29, s37, v29
	v_mbcnt_hi_u32_b32 v30, s39, v30
	v_mbcnt_hi_u32_b32 v31, s41, v31
	s_bcnt1_i32_b64 s54, s[34:35]
	s_bcnt1_i32_b64 s55, s[36:37]
	s_bcnt1_i32_b64 s56, s[38:39]
	s_bcnt1_i32_b64 s57, s[40:41]
	s_lshl2_add_u32 s58, s42, s46
	v_lshl_add_u32 v28, v28, 2, s58
	s_lshl2_add_u32 s58, s54, s58
	v_lshl_add_u32 v29, v29, 2, s58
	s_lshl2_add_u32 s58, s55, s58
	v_lshl_add_u32 v30, v30, 2, s58
	s_lshl2_add_u32 s58, s56, s58
	v_lshl_add_u32 v31, v31, 2, s58
	s_add_i32 s54, s54, s55
	s_add_i32 s56, s56, s57
	s_add_i32 s42, s42, s54
	s_add_i32 s42, s42, s56
	s_mov_b64 exec, s[34:35]
	ds_write_b32 v28, v10
	s_mov_b64 exec, s[36:37]
	ds_write_b32 v29, v11
	s_mov_b64 exec, s[38:39]
	ds_write_b32 v30, v12
	s_mov_b64 exec, s[40:41]
	ds_write_b32 v31, v13
	s_mov_b64 exec, -1
	s_branch .Lh_loop_entry
.Lh_stage3:
	s_mov_b32 s47, 3
	s_sub_i32 s59, s42, s43
	s_cmp_lt_i32 s59, 1
	s_cbranch_scc1 .Lh_epilogue
	s_bfm_b64 exec, s59, 0
	s_branch .Lh_loop_first
.Lh_loop_entry:
	s_sub_i32 s59, s42, s43
	s_cmp_lt_i32 s59, 64
	s_cbranch_scc1 .Lh_loop_exit
.Lh_loop_first:
	ds_read_b32 v24, v26
	s_waitcnt lgkmcnt(0)
.Lh_loop_body:
	v_fmamk_f32 v27, v24, 0x42000000, v41
	v_add_u32_e32 v26, 0x100, v26
	ds_read_b32 v24, v26
	s_sub_i32 s49, s44, s43
	s_sub_i32 s50, s45, s43
	s_add_i32 s43, s43, 64
	v_rndne_f32_e32 v28, v27
	v_cmp_le_i32_e32 vcc, s49, v1
	v_cmp_le_i32_e64 s[52:53], s50, v1
	v_sub_f32_e32 v29, v27, v28
	v_cvt_i32_f32_e32 v30, v28
	v_cndmask_b32_e32 v36, v38, v39, vcc
	v_mul_f32_e32 v37, 0xbf38aa3b, v29
	v_cndmask_b32_e64 v36, v36, v40, s[52:53]
	v_fmamk_f32 v32, v29, 0x3fb8aa3b, v42
	v_fma_f32 v33, -v29, s51, v42
	v_fmaak_f32 v31, v29, v37, 0x41a00000
	v_lshl_add_u32 v30, v30, 6, v36
	v_exp_f32_e32 v31, v31
	v_exp_f32_e32 v32, v32
	v_exp_f32_e32 v33, v33
	v_cvt_rpi_i32_f32_e32 v36, v31
	ds_add_u32 v30, v36 offset:320
	v_mul_f32_e32 v34, v32, v31
	v_mul_f32_e32 v35, v33, v31
	v_cvt_rpi_i32_f32_e32 v36, v34
	v_cvt_rpi_i32_f32_e32 v37, v35
	ds_add_u32 v30, v36 offset:384
	ds_add_u32 v30, v37 offset:256
	v_mul_f32_e32 v32, 0x3ebc5ab2, v32
	v_mul_f32_e32 v33, 0x3ebc5ab2, v33
	v_mul_f32_e32 v34, v32, v34
	v_mul_f32_e32 v35, v33, v35
	v_cvt_rpi_i32_f32_e32 v36, v34
	v_cvt_rpi_i32_f32_e32 v37, v35
	ds_add_u32 v30, v36 offset:448
	ds_add_u32 v30, v37 offset:192
	v_mul_f32_e32 v32, 0x3ebc5ab2, v32
	v_mul_f32_e32 v33, 0x3ebc5ab2, v33
	v_mul_f32_e32 v34, v32, v34
	v_mul_f32_e32 v35, v33, v35
	v_cvt_rpi_i32_f32_e32 v36, v34
	v_cvt_rpi_i32_f32_e32 v37, v35
	ds_add_u32 v30, v36 offset:512
	ds_add_u32 v30, v37 offset:128
	v_mul_f32_e32 v32, 0x3ebc5ab2, v32
	v_mul_f32_e32 v33, 0x3ebc5ab2, v33
	v_mul_f32_e32 v34, v32, v34
	v_mul_f32_e32 v35, v33, v35
	v_cvt_rpi_i32_f32_e32 v36, v34
	v_cvt_rpi_i32_f32_e32 v37, v35
	ds_add_u32 v30, v36 offset:576
	ds_add_u32 v30, v37 offset:64
	v_mul_f32_e32 v32, 0x3ebc5ab2, v32
	v_mul_f32_e32 v33, 0x3ebc5ab2, v33
	v_mul_f32_e32 v34, v32, v34
	v_mul_f32_e32 v35, v33, v35
	v_cvt_rpi_i32_f32_e32 v36, v34
	v_cvt_rpi_i32_f32_e32 v37, v35
	ds_add_u32 v30, v36 offset:640
	ds_add_u32 v30, v37
	s_sub_i32 s59, s42, s43
	s_cmp_ge_i32 s59, 64
	s_waitcnt lgkmcnt(11)
	s_cbranch_scc1 .Lh_loop_body
.Lh_loop_exit:
	s_cmp_eq_u32 s47, 0
	s_cbranch_scc1 .Lh_stage1
	s_cmp_eq_u32 s47, 1
	s_cbranch_scc1 .Lh_stage2
	s_cmp_eq_u32 s47, 2
	s_cbranch_scc1 .Lh_stage3
.Lh_epilogue:
	s_mov_b64 exec, -1
	s_waitcnt lgkmcnt(0)
	s_barrier
	s_cmp_gt_u32 s3, 6
	s_cbranch_scc1 .Lh_end
	s_cmp_eq_u32 s3, 6
	s_cbranch_scc1 .Lh_pcnt
	ds_read_b128 v[2:5], v45
	ds_read_b128 v[6:9], v46
	ds_read_b128 v[10:13], v47
	ds_read_b128 v[14:17], v48
	s_waitcnt lgkmcnt(2)
	v_add3_u32 v2, v2, v3, v4
	v_add3_u32 v5, v5, v6, v7
	s_waitcnt lgkmcnt(1)
	v_add3_u32 v8, v8, v9, v10
	v_add3_u32 v11, v11, v12, v13
	s_waitcnt lgkmcnt(0)
	v_add3_u32 v14, v14, v15, v16
	v_add3_u32 v2, v2, v5, v8
	v_add3_u32 v11, v11, v14, v17
	v_add_u32_e32 v2, v2, v11
	v_cvt_f32_u32_e32 v2, v2
	v_mul_f32_e32 v2, 0x35800000, v2
	global_store_dword v49, v2, s[10:11]
	s_endpgm
.Lh_pcnt:
	s_mov_b64 exec, 1
	ds_read_b128 v[2:5], v20
	ds_read_b128 v[6:9], v20 offset:16
	s_waitcnt lgkmcnt(1)
	v_add3_u32 v2, v2, v3, v4
	s_waitcnt lgkmcnt(0)
	v_add3_u32 v5, v5, v6, v7
	v_add3_u32 v2, v2, v5, v8
	v_add_u32_e32 v2, v2, v9
	global_store_dword v20, v2, s[12:13]

	.amdhsa_kernel _Z6k_histPKfS0_S0_PfPiS1_
		.amdhsa_group_segment_fixed_size 32
		.amdhsa_private_segment_fixed_size 0
		.amdhsa_kernarg_size 48
		.amdhsa_user_sgpr_count 2
		.amdhsa_user_sgpr_dispatch_ptr 0
		.amdhsa_user_sgpr_queue_ptr 0
		.amdhsa_user_sgpr_kernarg_segment_ptr 1
		.amdhsa_user_sgpr_dispatch_id 0
		.amdhsa_user_sgpr_kernarg_preload_length 0
		.amdhsa_user_sgpr_kernarg_preload_offset 0
		.amdhsa_user_sgpr_private_segment_size 0
		.amdhsa_uses_dynamic_stack 0
		.amdhsa_enable_private_segment 0
		.amdhsa_system_sgpr_workgroup_id_x 1
		.amdhsa_system_sgpr_workgroup_id_y 0
		.amdhsa_system_sgpr_workgroup_id_z 0
		.amdhsa_system_sgpr_workgroup_info 0
		.amdhsa_system_vgpr_workitem_id 0
		.amdhsa_next_free_vgpr 50
		.amdhsa_next_free_sgpr 60
		.amdhsa_accum_offset 52
		.amdhsa_reserve_vcc 1
		.amdhsa_float_round_mode_32 0
		.amdhsa_float_round_mode_16_64 0
		.amdhsa_float_denorm_mode_32 3
		.amdhsa_float_denorm_mode_16_64 3
		.amdhsa_dx10_clamp 1
		.amdhsa_ieee_mode 1
		.amdhsa_fp16_overflow 0
		.amdhsa_tg_split 0
		.amdhsa_exception_fp_ieee_invalid_op 0
		.amdhsa_exception_fp_denorm_src 0
		.amdhsa_exception_fp_ieee_div_zero 0
		.amdhsa_exception_fp_ieee_overflow 0
		.amdhsa_exception_fp_ieee_underflow 0
		.amdhsa_exception_fp_ieee_inexact 0
		.amdhsa_exception_int_div_zero 0
	.end_amdhsa_kernel

.Lfunc_end0:
	.size	_Z6k_histPKfS0_S0_PfPiS1_, .Lfunc_end0-_Z6k_histPKfS0_S0_PfPiS1_
	.set _Z6k_histPKfS0_S0_PfPiS1_.num_vgpr, 50
	.set _Z6k_histPKfS0_S0_PfPiS1_.num_agpr, 0
	.set _Z6k_histPKfS0_S0_PfPiS1_.numbered_sgpr, 60
	.set _Z6k_histPKfS0_S0_PfPiS1_.num_named_barrier, 0
	.set _Z6k_histPKfS0_S0_PfPiS1_.private_seg_size, 0
	.set _Z6k_histPKfS0_S0_PfPiS1_.uses_vcc, 1
	.set _Z6k_histPKfS0_S0_PfPiS1_.uses_flat_scratch, 0
	.set _Z6k_histPKfS0_S0_PfPiS1_.has_dyn_sized_stack, 0
	.set _Z6k_histPKfS0_S0_PfPiS1_.has_recursion, 0
	.set _Z6k_histPKfS0_S0_PfPiS1_.has_indirect_call, 0

amdhsa.kernels:
  - .agpr_count:     0
    .args:
      - .actual_access:  read_only
        .address_space:  global
        .offset:         0
        .size:           8
        .value_kind:     global_buffer
      - .actual_access:  read_only
        .address_space:  global
        .offset:         8
        .size:           8
        .value_kind:     global_buffer
      - .actual_access:  read_only
        .address_space:  global
        .offset:         16
        .size:           8
        .value_kind:     global_buffer
      - .actual_access:  write_only
        .address_space:  global
        .offset:         24
        .size:           8
        .value_kind:     global_buffer
      - .actual_access:  write_only
        .address_space:  global
        .offset:         32
        .size:           8
        .value_kind:     global_buffer
      - .actual_access:  write_only
        .address_space:  global
        .offset:         40
        .size:           8
        .value_kind:     global_buffer
    .group_segment_fixed_size: 32
    .kernarg_segment_align: 8
    .kernarg_segment_size: 48
    .language:       OpenCL C
    .language_version:
      - 2
      - 0
    .max_flat_workgroup_size: 1024
    .name:           _Z6k_histPKfS0_S0_PfPiS1_
    .private_segment_fixed_size: 0
    .sgpr_count:     66
    .sgpr_spill_count: 0
    .symbol:         _Z6k_histPKfS0_S0_PfPiS1_.kd
    .uniform_work_group_size: 1
    .uses_dynamic_stack: false
    .vgpr_count:     50
    .vgpr_spill_count: 0
    .wavefront_size: 64
  - .agpr_count:     0
    .args:
      - .actual_access:  read_only
        .address_space:  global
        .offset:         0
        .size:           8
        .value_kind:     global_buffer
      - .actual_access:  read_only
        .address_space:  global
        .offset:         8
        .size:           8
        .value_kind:     global_buffer
      - .address_space:  global
        .offset:         16
        .size:           8
        .value_kind:     global_buffer
    .group_segment_fixed_size: 2080
    .kernarg_segment_align: 8
    .kernarg_segment_size: 24
    .language:       OpenCL C
    .language_version:
      - 2
      - 0
    .max_flat_workgroup_size: 256
    .name:           _Z7k_finalPKfPKiPf
    .private_segment_fixed_size: 0
    .sgpr_count:     18
    .sgpr_spill_count: 0
    .symbol:         _Z7k_finalPKfPKiPf.kd
    .uniform_work_group_size: 1
    .uses_dynamic_stack: false
    .vgpr_count:     40
    .vgpr_spill_count: 0
    .wavefront_size: 64
